# v26
# speedup vs baseline: 1.0178x; 1.0054x over previous
.LBB0_5:
	v_mad_legacy_u16 v2, v6, s8, v4
	v_lshlrev_b16_e32 v8, 15, v2
	v_lshrrev_b16_e32 v2, 1, v2
	v_cmp_lt_u32_e32 vcc, s24, v6
	v_or_b32_e32 v2, v2, v8
	s_or_b64 s[0:1], vcc, s[0:1]
	v_cmp_gt_u16_e32 vcc, s9, v2
	v_add_u32_e32 v7, 0x200, v6
	v_mov_b32_e32 v6, v7
	v_cndmask_b32_e32 v2, 0, v5, vcc
	ds_write_b64 v1, v[2:3]
	v_add_u32_e32 v1, 0x1000, v1
	s_andn2_b64 exec, exec, s[0:1]
	s_cbranch_execnz .LBB0_5
	s_or_b64 exec, exec, s[0:1]
	s_mov_b32 s34, 0
	v_cmp_eq_u32_e64 s[0:1], 0, v0
	s_and_saveexec_b64 s[8:9], s[0:1]
	v_mov_b32_e32 v1, 8
	v_mov_b32_e32 v2, 0x23420
	ds_write_b32 v2, v1
	s_or_b64 exec, exec, s[8:9]
	v_lshlrev_b32_e32 v1, 2, v131
	v_or_b32_e32 v2, 0x22200, v1
	v_or_b32_e32 v3, 0x22300, v1
	v_mbcnt_lo_u32_b32 v238, -1, 0
	v_mbcnt_hi_u32_b32 v238, -1, v238
	v_and_b32_e32 v239, 64, v238
	v_add_u32_e32 v239, 64, v239
	v_xor_b32_e32 v240, 32, v238
	v_cmp_lt_i32_e32 vcc, v240, v239
	v_mov_b32_e32 v133, 0
	v_lshrrev_b32_e32 v209, 4, v131
	v_cndmask_b32_e32 v240, v238, v240, vcc
	v_lshlrev_b32_e32 v200, 2, v240
	v_and_b32_e32 v203, 48, v0
	v_xor_b32_e32 v240, 16, v238
	v_cmp_lt_i32_e32 vcc, v240, v239
	v_cndmask_b32_e32 v240, v238, v240, vcc
	v_lshlrev_b32_e32 v201, 2, v240
	v_xor_b32_e32 v240, 8, v238
	v_cmp_lt_i32_e32 vcc, v240, v239
	v_cndmask_b32_e32 v240, v238, v240, vcc
	v_lshlrev_b32_e32 v205, 2, v240
	v_cmp_eq_u32_e64 s[8:9], 0, v131
	v_mov_b32_e32 v218, 0xff800000
	v_mov_b32_e32 v213, 0x23420
	v_xor_b32_e32 v240, 4, v238
	v_cmp_lt_i32_e32 vcc, v240, v239
	v_cndmask_b32_e32 v240, v238, v240, vcc
	v_lshlrev_b32_e32 v206, 2, v240
	v_xor_b32_e32 v240, 2, v238
	v_cmp_lt_i32_e32 vcc, v240, v239
	v_mov_b32_e32 v219, 0
	s_mov_b32 s35, s31
	v_cndmask_b32_e32 v240, v238, v240, vcc
	v_lshlrev_b32_e32 v207, 2, v240
	v_mov_b32_e32 v138, 0
	v_mov_b32_e32 v139, v133
	v_mov_b32_e32 v136, 0
	v_mov_b32_e32 v137, v133
	v_xor_b32_e32 v240, 1, v238
	v_cmp_lt_i32_e32 vcc, v240, v239
	v_cndmask_b32_e32 v238, v238, v240, vcc
	v_lshlrev_b32_e32 v208, 2, v238
	v_mov_b32_e32 v150, 0
	s_waitcnt lgkmcnt(0)
	s_barrier
	ds_read_b32 v2, v2
	ds_read_b32 v3, v3
	v_and_b32_e32 v202, 15, v0
	s_lshl_b32 s30, s31, 4
	v_or_b32_e32 v132, s30, v202
	s_waitcnt lgkmcnt(0)
	v_add_f32_e32 v2, v2, v3
	v_lshlrev_b32_e32 v4, 3, v131
	s_nop 1
	v_add_f32_dpp v2, v2, v2 row_shr:1 row_mask:0xf bank_mask:0xf
	s_nop 1
	v_add_f32_dpp v2, v2, v2 row_shr:2 row_mask:0xf bank_mask:0xf
	s_nop 1
	v_add_f32_dpp v2, v2, v2 row_shr:4 row_mask:0xf bank_mask:0xf
	s_nop 1
	v_add_f32_dpp v2, v2, v2 row_shr:8 row_mask:0xf bank_mask:0xf
	s_nop 1
	v_add_f32_dpp v2, v2, v2 row_bcast:15 row_mask:0xa bank_mask:0xf
	s_nop 1
	v_add_f32_dpp v2, v2, v2 row_bcast:31 row_mask:0xc bank_mask:0xf
	s_nop 1
	v_readlane_b32 s44, v2, 63
	s_nop 1
	v_mov_b32_e32 v2, s44
	v_add_f32_e32 v2, s43, v2
	s_mul_i32 s4, s31, 0x2200
	s_add_i32 s24, s4, 0x11000
	v_mul_f32_e32 v210, 0x3fb8aa3b, v2
	s_movk_i32 s4, 0x220
	v_mov_b32_e32 v2, s24
	v_mad_u32_u24 v5, v202, s4, v2
	v_lshlrev_b64 v[2:3], 9, v[132:133]
	v_lshl_add_u64 v[2:3], s[6:7], 0, v[2:3]
	v_lshlrev_b32_e32 v132, 5, v209
	v_add_u32_e32 v212, s24, v4
	v_mad_u32_u24 v211, v202, s4, v203
	v_lshl_add_u64 v[134:135], v[2:3], 0, v[132:133]
	v_cmp_eq_u32_e64 s[6:7], 15, v202
	v_cmp_eq_u32_e64 s[4:5], 15, v131
	v_add_u32_e32 v214, v5, v203
	v_add_u32_e32 v215, 0x800, v212
	v_add_u32_e32 v216, 0x1000, v212
	v_add_u32_e32 v217, 0x1800, v212
	v_mov_b32_e32 v151, v133
	v_mov_b32_e32 v140, 0
	v_mov_b32_e32 v141, v133
	v_mov_b32_e32 v178, 0
	v_mov_b32_e32 v179, v133
	v_mov_b32_e32 v168, 0
	v_mov_b32_e32 v169, v133
	v_mov_b32_e32 v182, 0
	v_mov_b32_e32 v183, v133
	v_mov_b32_e32 v180, 0
	v_mov_b32_e32 v181, v133
	v_mov_b32_e32 v186, 0
	v_mov_b32_e32 v187, v133
	v_mov_b32_e32 v184, 0
	v_mov_b32_e32 v185, v133
	v_mov_b32_e32 v190, 0
	v_mov_b32_e32 v191, v133
	v_mov_b32_e32 v188, 0
	v_mov_b32_e32 v189, v133
	v_mov_b32_e32 v194, 0
	v_mov_b32_e32 v195, v133
	v_mov_b32_e32 v192, 0
	v_mov_b32_e32 v193, v133
	v_mov_b32_e32 v198, 0
	v_mov_b32_e32 v199, v133
	v_mov_b32_e32 v196, 0
	v_mov_b32_e32 v197, v133
	s_cmp_eq_u32 s2, 0
	s_cselect_b64 s[24:25], -1, 0
	s_and_b64 s[24:25], s[24:25], s[10:11]
	s_and_saveexec_b64 s[26:27], s[24:25]
	s_cbranch_execz .Lp1_noinit
	global_store_dword v[254:255], v253, off
